# row passes 1/2: streaming (nt) hint on the X / H / H8 / out stores
# speedup vs baseline: 1.0005x; 1.0005x over previous
; #define RP_UNPK(V_, H_) ((H_) ? (f32x4){bflo((V_)[2]), bfhi((V_)[2]), bflo((V_)[3]), bfhi((V_)[3])} : (f32x4){bflo((V_)[0]), bfhi((V_)[0]), bflo((V_)[1]), bfhi((V_)[1])})
; template <int MODE, bool FIRSTX>
; __device__ __forceinline__ void row_pass(Frame& F, int layer, bool final_out, int row0) {
;     ...
;         f32x4 v[4];
; #pragma unroll
;         for (int q = 0; q < 4; ++q) v[q] = FIRSTX ? xf[q] : RP_UNPK(xb[q >> 1], q & 1);
;         if (MODE != 0) {
; #pragma unroll
;             for (int q = 0; q < 4; ++q) { f32x4 y = (f32x4){0.f, 0.f, 0.f, 0.f};
; #pragma unroll
;                 for (int k = 0; k < NY; ++k) { if (MODE == 2) { const unsigned w8 = yb[k][q >> 1][q & 1]; const f32x2 lo = __builtin_amdgcn_cvt_pk_f32_fp8((int)w8, false), hi = __builtin_amdgcn_cvt_pk_f32_fp8((int)w8, true); y += (f32x4){lo.x, lo.y, hi.x, hi.y}; }
;                                                 else y += RP_UNPK(yb[k][q >> 1], q & 1); }
;                 if (MODE == 2) y = y * (1.0f / YK8_SCALE);
;                 v[q] = v[q] * DN_ALPHA + gt[q] * y; }
;             float s = 0.f;
; #pragma unroll
;             for (int q = 0; q < 4; ++q) s += (v[q][0] + v[q][1]) + (v[q][2] + v[q][3]);
;             const float mean = wave_sum(s) * (1.0f / DM); float qq = 0.f;
; #pragma unroll
;             for (int q = 0; q < 4; ++q) { v[q] = v[q] - mean; qq += (v[q][0] * v[q][0] + v[q][1] * v[q][1]) + (v[q][2] * v[q][2] + v[q][3] * v[q][3]); }
;             const float rstd = 1.0f / sqrtf(wave_sum(qq) * (1.0f / DM) + LN_EPS);
.Lrp1_common:
	v_lshlrev_b32_e32 v128, 16, v102
	v_and_b32_e32 v129, 0xffff0000, v102
	v_lshlrev_b32_e32 v102, 16, v103
	v_and_b32_e32 v103, 0xffff0000, v103
	v_pk_add_f32 v[102:103], v[102:103], 0 op_sel_hi:[1,0]
	v_pk_add_f32 v[128:129], v[128:129], 0 op_sel_hi:[1,0]
	v_lshlrev_b32_e32 v120, 16, v110
	v_and_b32_e32 v121, 0xffff0000, v110
	v_lshlrev_b32_e32 v110, 16, v111
	v_and_b32_e32 v111, 0xffff0000, v111
	v_pk_mul_f32 v[128:129], v[128:129], v[46:47]
	v_pk_mul_f32 v[102:103], v[102:103], v[48:49]
	v_lshlrev_b32_e32 v122, 16, v112
	v_pk_fma_f32 v[102:103], v[110:111], s[62:63], v[102:103] op_sel_hi:[1,0,1]
	v_pk_fma_f32 v[110:111], v[120:121], s[62:63], v[128:129] op_sel_hi:[1,0,1]
	v_lshlrev_b32_e32 v120, 16, v104
	v_and_b32_e32 v121, 0xffff0000, v104
	v_lshlrev_b32_e32 v104, 16, v105
	v_and_b32_e32 v105, 0xffff0000, v105
	v_pk_add_f32 v[104:105], v[104:105], 0 op_sel_hi:[1,0]
	v_pk_add_f32 v[120:121], v[120:121], 0 op_sel_hi:[1,0]
	v_and_b32_e32 v123, 0xffff0000, v112
	v_lshlrev_b32_e32 v112, 16, v113
	v_and_b32_e32 v113, 0xffff0000, v113
	v_pk_mul_f32 v[120:121], v[120:121], v[42:43]
	v_pk_mul_f32 v[104:105], v[104:105], v[44:45]
	v_lshlrev_b32_e32 v124, 16, v106
	v_pk_fma_f32 v[104:105], v[112:113], s[62:63], v[104:105] op_sel_hi:[1,0,1]
	v_pk_fma_f32 v[112:113], v[122:123], s[62:63], v[120:121] op_sel_hi:[1,0,1]
	v_lshlrev_b32_e32 v120, 16, v98
	v_and_b32_e32 v121, 0xffff0000, v98
	v_lshlrev_b32_e32 v98, 16, v99
	v_and_b32_e32 v99, 0xffff0000, v99
	v_pk_add_f32 v[98:99], v[98:99], 0 op_sel_hi:[1,0]
	v_pk_add_f32 v[120:121], v[120:121], 0 op_sel_hi:[1,0]
	v_and_b32_e32 v125, 0xffff0000, v106
	v_lshlrev_b32_e32 v106, 16, v107
	v_and_b32_e32 v107, 0xffff0000, v107
	v_pk_mul_f32 v[120:121], v[120:121], v[78:79]
	v_pk_mul_f32 v[98:99], v[98:99], v[80:81]
	v_lshlrev_b32_e32 v126, 16, v108
	v_pk_fma_f32 v[98:99], v[106:107], s[62:63], v[98:99] op_sel_hi:[1,0,1]
	v_pk_fma_f32 v[106:107], v[124:125], s[62:63], v[120:121] op_sel_hi:[1,0,1]
	v_lshlrev_b32_e32 v120, 16, v100
	v_and_b32_e32 v121, 0xffff0000, v100
	v_lshlrev_b32_e32 v100, 16, v101
	v_and_b32_e32 v101, 0xffff0000, v101
	v_pk_add_f32 v[100:101], v[100:101], 0 op_sel_hi:[1,0]
	v_pk_add_f32 v[120:121], v[120:121], 0 op_sel_hi:[1,0]
	v_and_b32_e32 v127, 0xffff0000, v108
	v_lshlrev_b32_e32 v108, 16, v109
	v_and_b32_e32 v109, 0xffff0000, v109
	v_pk_mul_f32 v[120:121], v[120:121], v[70:71]
	v_pk_mul_f32 v[100:101], v[100:101], v[72:73]
	v_add_f32_e32 v122, v104, v105
	v_pk_fma_f32 v[100:101], v[108:109], s[62:63], v[100:101] op_sel_hi:[1,0,1]
	v_pk_fma_f32 v[108:109], v[126:127], s[62:63], v[120:121] op_sel_hi:[1,0,1]
	v_add_f32_e32 v120, v110, v111
	v_add_f32_e32 v121, v102, v103
	v_add_f32_e32 v120, v120, v121
	v_add_f32_e32 v121, v112, v113
	v_add_f32_e32 v120, 0, v120
	v_add_f32_e32 v121, v121, v122
	v_add_f32_e32 v120, v121, v120
	v_add_f32_e32 v121, v106, v107
	v_add_f32_e32 v122, v98, v99
	v_add_f32_e32 v121, v121, v122
	v_add_f32_e32 v120, v121, v120
	v_add_f32_e32 v121, v108, v109
	v_add_f32_e32 v122, v100, v101
	v_add_f32_e32 v121, v121, v122
	v_add_f32_e32 v120, v121, v120
	ds_swizzle_b32 v121, v120 offset:swizzle(SWAP,1)
	s_add_i32 s11, s11, 1
	v_lshl_add_u64 v[118:119], v[118:119], 0, s[50:51]
	s_cmp_lt_i32 s1, s14
	s_waitcnt lgkmcnt(0)
	v_add_f32_e32 v120, v120, v121
	ds_swizzle_b32 v121, v120 offset:swizzle(SWAP,2)
	s_waitcnt lgkmcnt(0)
	v_add_f32_e32 v120, v120, v121
	ds_swizzle_b32 v121, v120 offset:swizzle(SWAP,4)
	s_waitcnt lgkmcnt(0)
	v_add_f32_e32 v120, v120, v121
	ds_swizzle_b32 v121, v120 offset:swizzle(SWAP,8)
	s_waitcnt lgkmcnt(0)
	v_add_f32_e32 v120, v120, v121
	ds_swizzle_b32 v121, v120 offset:swizzle(SWAP,16)
	s_waitcnt lgkmcnt(0)
	v_add_f32_e32 v120, v120, v121
	v_mov_b32_e32 v121, v120
	s_nop 1
	v_permlane32_swap_b32_e32 v120, v121
	v_add_f32_e32 v120, v120, v121
	v_fmac_f32_e32 v103, 0xba800000, v120
	v_fmac_f32_e32 v111, 0xba800000, v120
	v_fmamk_f32 v102, v120, 0xba800000, v102
	v_fmamk_f32 v110, v120, 0xba800000, v110
	v_mul_f32_e32 v121, v111, v111
	v_mul_f32_e32 v122, v103, v103
	v_fmac_f32_e32 v121, v110, v110
	v_fmac_f32_e32 v122, v102, v102
	v_fmac_f32_e32 v105, 0xba800000, v120
	v_fmac_f32_e32 v113, 0xba800000, v120
	v_add_f32_e32 v121, v121, v122
	v_fmamk_f32 v104, v120, 0xba800000, v104
	v_fmamk_f32 v112, v120, 0xba800000, v112
	v_mul_f32_e32 v122, v113, v113
	v_mul_f32_e32 v123, v105, v105
	v_fmac_f32_e32 v122, v112, v112
	v_fmac_f32_e32 v123, v104, v104
	v_add_f32_e32 v122, v122, v123
	v_fmac_f32_e32 v99, 0xba800000, v120
	v_fmac_f32_e32 v107, 0xba800000, v120
	v_add_f32_e32 v121, v121, v122
	v_fmamk_f32 v98, v120, 0xba800000, v98
	v_fmamk_f32 v106, v120, 0xba800000, v106
	v_mul_f32_e32 v122, v107, v107
	v_mul_f32_e32 v123, v99, v99
	v_fmac_f32_e32 v122, v106, v106
	v_fmac_f32_e32 v123, v98, v98
	v_add_f32_e32 v122, v122, v123
	v_fmac_f32_e32 v101, 0xba800000, v120
	v_fmac_f32_e32 v109, 0xba800000, v120
	v_add_f32_e32 v121, v122, v121
	v_fmamk_f32 v100, v120, 0xba800000, v100
	v_fmamk_f32 v108, v120, 0xba800000, v108
	v_mul_f32_e32 v120, v109, v109
	v_mul_f32_e32 v122, v101, v101
	v_fmac_f32_e32 v120, v108, v108
	v_fmac_f32_e32 v122, v100, v100
	v_add_f32_e32 v120, v120, v122
	v_add_f32_e32 v120, v120, v121
	ds_swizzle_b32 v121, v120 offset:swizzle(SWAP,1)
	s_waitcnt lgkmcnt(0)
	v_add_f32_e32 v120, v120, v121
	ds_swizzle_b32 v121, v120 offset:swizzle(SWAP,2)
	s_waitcnt lgkmcnt(0)
	v_add_f32_e32 v120, v120, v121
	ds_swizzle_b32 v121, v120 offset:swizzle(SWAP,4)
	s_waitcnt lgkmcnt(0)
	v_add_f32_e32 v120, v120, v121
	ds_swizzle_b32 v121, v120 offset:swizzle(SWAP,8)
	s_waitcnt lgkmcnt(0)
	v_add_f32_e32 v120, v120, v121
	ds_swizzle_b32 v121, v120 offset:swizzle(SWAP,16)
	s_waitcnt lgkmcnt(0)
; __device__ __forceinline__ unsigned pk2(float lo, float hi) { return f2bf(lo) | (f2bf(hi) << 16); }
; __device__ __forceinline__ unsigned cvt_fp8x4(float a, float b, float c, float d) { int w = __builtin_amdgcn_cvt_pk_fp8_f32(a, b, 0, false); w = __builtin_amdgcn_cvt_pk_fp8_f32(c, d, w, true); return (unsigned)w; }
; template <int MODE, bool FIRSTX>
; __device__ __forceinline__ void row_pass(Frame& F, int layer, bool final_out, int row0) {
;     ...
;             const float rstd = 1.0f / sqrtf(wave_sum(qq) * (1.0f / DM) + LN_EPS);
; #pragma unroll
;             for (int q = 0; q < 4; ++q) v[q] = v[q] * rstd * lg[q] + lb[q];
;             if (final_out) { if (row >= NCTX) {
; #pragma unroll
;                 for (int q = 0; q < 4; ++q) *(f32x4*)(F.out + (size_t)(row - NCTX) * DM + RP_COL(q)) = v[q]; } }
;             else {
; #pragma unroll
;                 for (int j = 0; j < 2; ++j) { u32x4 w; w.x = pk2(v[2 * j][0], v[2 * j][1]); w.y = pk2(v[2 * j][2], v[2 * j][3]); w.z = pk2(v[2 * j + 1][0], v[2 * j + 1][1]); w.w = pk2(v[2 * j + 1][2], v[2 * j + 1][3]);
;                     *(u32x4*)(X + (size_t)row * DM + lc + 512 * j) = w; } }
;         }
;         if (!final_out) {
; #pragma unroll
;             for (int j = 0; j < 2; ++j) { const f32x4 h0 = v[2 * j] * (sc[2 * j] + 1.0f) + sh[2 * j], h1 = v[2 * j + 1] * (sc[2 * j + 1] + 1.0f) + sh[2 * j + 1];
;                 if (MODE == 1 || (nlayer % 3) == 2) { u32x4 w; w.x = pk2(h0[0], h0[1]); w.y = pk2(h0[2], h0[3]); w.z = pk2(h1[0], h1[1]); w.w = pk2(h1[2], h1[3]);
;                     *(u32x4*)(H + (size_t)row * DM + lc + 512 * j) = w; }
;                 if (MODE == 1 || (nlayer % 3) != 2) {                                u32x2 w8; w8.x = cvt_fp8x4(h0[0], h0[1], h0[2], h0[3]); w8.y = cvt_fp8x4(h1[0], h1[1], h1[2], h1[3]); *(u32x2*)(F.ws + WS_H8 + (size_t)row * DM + lc + 512 * j) = w8; } }
	v_add_f32_e32 v120, v120, v121
	v_mov_b32_e32 v121, v120
	s_nop 1
	v_permlane32_swap_b32_e32 v120, v121
	v_add_f32_e32 v120, v120, v121
	v_fmamk_f32 v120, v120, 0x3a800000, v188
	v_mul_f32_e32 v121, 0x4f800000, v120
	v_cmp_gt_f32_e32 vcc, s31, v120
	s_nop 1
	v_cndmask_b32_e32 v120, v120, v121, vcc
	v_sqrt_f32_e32 v121, v120
	s_nop 0
	v_add_u32_e32 v122, -1, v121
	v_fma_f32 v123, -v122, v121, v120
	v_cmp_ge_f32_e64 s[2:3], 0, v123
	v_add_u32_e32 v123, 1, v121
	s_nop 0
	v_cndmask_b32_e64 v122, v121, v122, s[2:3]
	v_fma_f32 v121, -v123, v121, v120
	v_cmp_lt_f32_e64 s[2:3], 0, v121
	s_nop 1
	v_cndmask_b32_e64 v121, v122, v123, s[2:3]
	v_mul_f32_e32 v122, 0x37800000, v121
	v_cndmask_b32_e32 v121, v121, v122, vcc
	v_cmp_class_f32_e32 vcc, v120, v189
	s_nop 1
	v_cndmask_b32_e32 v120, v121, v120, vcc
	v_div_scale_f32 v121, s[2:3], v120, v120, 1.0
	v_rcp_f32_e32 v122, v121
	s_nop 0
	v_fma_f32 v123, -v121, v122, 1.0
	v_fmac_f32_e32 v122, v123, v122
	v_div_scale_f32 v123, vcc, 1.0, v120, 1.0
	v_mul_f32_e32 v124, v123, v122
	v_fma_f32 v125, -v121, v124, v123
	v_fmac_f32_e32 v124, v125, v122
	v_fma_f32 v121, -v121, v124, v123
	v_div_fmas_f32 v121, v121, v122, v124
	v_div_fixup_f32 v120, v121, v120, 1.0
	v_pk_mul_f32 v[110:111], v[110:111], v[120:121] op_sel_hi:[1,0]
	v_pk_mul_f32 v[98:99], v[98:99], v[120:121] op_sel_hi:[1,0]
	v_pk_fma_f32 v[110:111], v[2:3], v[110:111], v[6:7]
	v_pk_fma_f32 v[122:123], v[20:21], v[98:99], v[24:25]
	v_pk_mul_f32 v[98:99], v[100:101], v[120:121] op_sel_hi:[1,0]
	v_pk_mul_f32 v[102:103], v[102:103], v[120:121] op_sel_hi:[1,0]
	v_pk_mul_f32 v[112:113], v[112:113], v[120:121] op_sel_hi:[1,0]
	v_pk_mul_f32 v[104:105], v[104:105], v[120:121] op_sel_hi:[1,0]
	v_pk_mul_f32 v[106:107], v[106:107], v[120:121] op_sel_hi:[1,0]
	v_pk_mul_f32 v[100:101], v[108:109], v[120:121] op_sel_hi:[1,0]
	v_pk_fma_f32 v[120:121], v[28:29], v[98:99], v[32:33]
	v_bfe_u32 v98, v110, 16, 1
	v_add3_u32 v98, v110, v98, s43
	v_bfe_u32 v99, v111, 16, 1
	v_pk_fma_f32 v[102:103], v[4:5], v[102:103], v[8:9]
	v_lshrrev_b32_e32 v98, 16, v98
	v_add3_u32 v99, v111, v99, s43
	v_and_or_b32 v98, v99, s33, v98
	v_bfe_u32 v99, v102, 16, 1
	v_pk_fma_f32 v[108:109], v[26:27], v[100:101], v[30:31]
	v_add3_u32 v99, v102, v99, s43
	v_bfe_u32 v100, v103, 16, 1
	v_pk_fma_f32 v[112:113], v[10:11], v[112:113], v[14:15]
	v_lshrrev_b32_e32 v99, 16, v99
	v_add3_u32 v100, v103, v100, s43
	v_and_or_b32 v99, v100, s33, v99
	v_bfe_u32 v100, v112, 16, 1
	v_add3_u32 v100, v112, v100, s43
	v_bfe_u32 v101, v113, 16, 1
	v_pk_fma_f32 v[104:105], v[12:13], v[104:105], v[16:17]
	v_lshrrev_b32_e32 v100, 16, v100
	v_add3_u32 v101, v113, v101, s43
	v_and_or_b32 v100, v101, s33, v100
	v_bfe_u32 v101, v104, 16, 1
	v_add3_u32 v101, v104, v101, s43
	v_bfe_u32 v126, v105, 16, 1
	v_lshl_add_u64 v[124:125], s[74:75], 0, v[114:115]
	v_lshrrev_b32_e32 v101, 16, v101
	v_add3_u32 v126, v105, v126, s43
	v_and_or_b32 v101, v126, s33, v101
	v_add_co_u32_e32 v126, vcc, s39, v124
	v_pk_fma_f32 v[106:107], v[18:19], v[106:107], v[22:23]
	s_nop 0
	v_addc_co_u32_e32 v127, vcc, 0, v125, vcc
	global_store_dwordx4 v[126:127], v[98:101], off nt
	v_bfe_u32 v128, v121, 16, 1
	v_add3_u32 v128, v121, v128, s43
	v_bfe_u32 v98, v106, 16, 1
	v_add3_u32 v98, v106, v98, s43
	v_bfe_u32 v99, v107, 16, 1
	v_lshrrev_b32_e32 v98, 16, v98
	v_add3_u32 v99, v107, v99, s43
	v_and_or_b32 v98, v99, s33, v98
	v_bfe_u32 v99, v122, 16, 1
	v_add3_u32 v99, v122, v99, s43
	v_bfe_u32 v100, v123, 16, 1
	v_lshrrev_b32_e32 v99, 16, v99
	v_add3_u32 v100, v123, v100, s43
	v_and_or_b32 v99, v100, s33, v99
	v_bfe_u32 v100, v108, 16, 1
	v_add3_u32 v100, v108, v100, s43
	v_bfe_u32 v101, v109, 16, 1
	v_lshrrev_b32_e32 v100, 16, v100
	v_add3_u32 v101, v109, v101, s43
	v_and_or_b32 v100, v101, s33, v100
	v_bfe_u32 v101, v120, 16, 1
	v_add3_u32 v101, v120, v101, s43
	v_lshrrev_b32_e32 v101, 16, v101
	v_and_or_b32 v101, v128, s33, v101
	global_store_dwordx4 v[126:127], v[98:101], off offset:1024 nt
	v_lshl_add_u64 v[114:115], v[114:115], 0, s[50:51]
	s_nop 0
	v_pk_add_f32 v[98:99], v[76:77], 1.0 op_sel_hi:[1,0]
	v_pk_add_f32 v[100:101], v[74:75], 1.0 op_sel_hi:[1,0]
	v_pk_fma_f32 v[102:103], v[98:99], v[102:103], v[64:65]
	v_pk_fma_f32 v[110:111], v[100:101], v[110:111], v[62:63]
	v_pk_add_f32 v[98:99], v[68:69], 1.0 op_sel_hi:[1,0]
	v_pk_add_f32 v[100:101], v[66:67], 1.0 op_sel_hi:[1,0]
	v_pk_fma_f32 v[104:105], v[98:99], v[104:105], v[60:61]
	v_and_b32_sdwa v99, v110, v185 dst_sel:DWORD dst_unused:UNUSED_PAD src0_sel:WORD_1 src1_sel:DWORD
	v_pk_fma_f32 v[112:113], v[100:101], v[112:113], v[58:59]
	v_add3_u32 v100, v110, v99, s43
	v_and_b32_sdwa v99, v103, v185 dst_sel:DWORD dst_unused:UNUSED_PAD src0_sel:WORD_1 src1_sel:DWORD
	v_and_b32_sdwa v101, v111, v185 dst_sel:DWORD dst_unused:UNUSED_PAD src0_sel:WORD_1 src1_sel:DWORD
; __device__ __forceinline__ unsigned pk2(float lo, float hi) { return f2bf(lo) | (f2bf(hi) << 16); }
; __device__ __forceinline__ unsigned cvt_fp8x4(float a, float b, float c, float d) { int w = __builtin_amdgcn_cvt_pk_fp8_f32(a, b, 0, false); w = __builtin_amdgcn_cvt_pk_fp8_f32(c, d, w, true); return (unsigned)w; }
; template <int MODE, bool FIRSTX>
; __device__ __forceinline__ void row_pass(Frame& F, int layer, bool final_out, int row0) {
;     ...
;                 for (int j = 0; j < 2; ++j) { u32x4 w; w.x = pk2(v[2 * j][0], v[2 * j][1]); w.y = pk2(v[2 * j][2], v[2 * j][3]); w.z = pk2(v[2 * j + 1][0], v[2 * j + 1][1]); w.w = pk2(v[2 * j + 1][2], v[2 * j + 1][3]);
;                     *(u32x4*)(X + (size_t)row * DM + lc + 512 * j) = w; } }
;         }
;         if (!final_out) {
; #pragma unroll
;             for (int j = 0; j < 2; ++j) { const f32x4 h0 = v[2 * j] * (sc[2 * j] + 1.0f) + sh[2 * j], h1 = v[2 * j + 1] * (sc[2 * j + 1] + 1.0f) + sh[2 * j + 1];
;                 if (MODE == 1 || (nlayer % 3) == 2) { u32x4 w; w.x = pk2(h0[0], h0[1]); w.y = pk2(h0[2], h0[3]); w.z = pk2(h1[0], h1[1]); w.w = pk2(h1[2], h1[3]);
;                     *(u32x4*)(H + (size_t)row * DM + lc + 512 * j) = w; }
;                 if (MODE == 1 || (nlayer % 3) != 2) {                                u32x2 w8; w8.x = cvt_fp8x4(h0[0], h0[1], h0[2], h0[3]); w8.y = cvt_fp8x4(h1[0], h1[1], h1[2], h1[3]); *(u32x2*)(F.ws + WS_H8 + (size_t)row * DM + lc + 512 * j) = w8; } }
	v_and_b32_sdwa v98, v102, v185 dst_sel:DWORD dst_unused:UNUSED_PAD src0_sel:WORD_1 src1_sel:DWORD
	v_add3_u32 v99, v103, v99, s43
	v_add3_u32 v101, v111, v101, s43
	v_add3_u32 v98, v102, v98, s43
	v_and_b32_e32 v99, 0xffff0000, v99
	v_and_b32_e32 v101, 0xffff0000, v101
	v_or_b32_sdwa v99, v99, v98 dst_sel:DWORD dst_unused:UNUSED_PAD src0_sel:DWORD src1_sel:WORD_1
	v_or_b32_sdwa v98, v101, v100 dst_sel:DWORD dst_unused:UNUSED_PAD src0_sel:DWORD src1_sel:WORD_1
	v_and_b32_sdwa v101, v112, v185 dst_sel:DWORD dst_unused:UNUSED_PAD src0_sel:WORD_1 src1_sel:DWORD
	v_add3_u32 v126, v112, v101, s43
	v_and_b32_sdwa v101, v105, v185 dst_sel:DWORD dst_unused:UNUSED_PAD src0_sel:WORD_1 src1_sel:DWORD
	v_and_b32_sdwa v127, v113, v185 dst_sel:DWORD dst_unused:UNUSED_PAD src0_sel:WORD_1 src1_sel:DWORD
	v_and_b32_sdwa v100, v104, v185 dst_sel:DWORD dst_unused:UNUSED_PAD src0_sel:WORD_1 src1_sel:DWORD
	v_add3_u32 v101, v105, v101, s43
	v_add3_u32 v127, v113, v127, s43
	v_add3_u32 v100, v104, v100, s43
	v_and_b32_e32 v101, 0xffff0000, v101
	v_and_b32_e32 v127, 0xffff0000, v127
	v_or_b32_sdwa v101, v101, v100 dst_sel:DWORD dst_unused:UNUSED_PAD src0_sel:DWORD src1_sel:WORD_1
	v_or_b32_sdwa v100, v127, v126 dst_sel:DWORD dst_unused:UNUSED_PAD src0_sel:DWORD src1_sel:WORD_1
	v_mov_b32_e32 v126, v1
	v_cvt_pk_fp8_f32 v126, v110, v111
	v_mov_b32_e32 v127, v1
	v_add_co_u32_e32 v110, vcc, s28, v124
	v_cvt_pk_fp8_f32 v127, v112, v113
	s_nop 0
	v_addc_co_u32_e32 v111, vcc, 0, v125, vcc
	global_store_dwordx4 v[110:111], v[98:101], off nt
	v_cvt_pk_fp8_f32 v126, v102, v103 op_sel:[0,0,1]
	v_cvt_pk_fp8_f32 v127, v104, v105 op_sel:[0,0,1]
	v_lshl_add_u64 v[98:99], s[74:75], 0, v[116:117]
	v_add_co_u32_e32 v102, vcc, s38, v98
	v_pk_add_f32 v[100:101], v[94:95], 1.0 op_sel_hi:[1,0]
	s_nop 0
	v_addc_co_u32_e32 v103, vcc, 0, v99, vcc
	v_pk_add_f32 v[98:99], v[96:97], 1.0 op_sel_hi:[1,0]
	v_pk_fma_f32 v[100:101], v[100:101], v[106:107], v[86:87]
	v_pk_fma_f32 v[104:105], v[98:99], v[122:123], v[88:89]
	v_pk_add_f32 v[98:99], v[92:93], 1.0 op_sel_hi:[1,0]
	v_pk_add_f32 v[106:107], v[90:91], 1.0 op_sel_hi:[1,0]
	v_pk_fma_f32 v[112:113], v[98:99], v[120:121], v[84:85]
	v_and_b32_sdwa v99, v100, v185 dst_sel:DWORD dst_unused:UNUSED_PAD src0_sel:WORD_1 src1_sel:DWORD
	v_pk_fma_f32 v[106:107], v[106:107], v[108:109], v[82:83]
	v_add3_u32 v108, v100, v99, s43
	v_and_b32_sdwa v99, v105, v185 dst_sel:DWORD dst_unused:UNUSED_PAD src0_sel:WORD_1 src1_sel:DWORD
	v_and_b32_sdwa v109, v101, v185 dst_sel:DWORD dst_unused:UNUSED_PAD src0_sel:WORD_1 src1_sel:DWORD
	v_and_b32_sdwa v98, v104, v185 dst_sel:DWORD dst_unused:UNUSED_PAD src0_sel:WORD_1 src1_sel:DWORD
	v_add3_u32 v99, v105, v99, s43
	v_add3_u32 v109, v101, v109, s43
	v_add3_u32 v98, v104, v98, s43
	v_and_b32_e32 v99, 0xffff0000, v99
	v_and_b32_e32 v109, 0xffff0000, v109
	v_or_b32_sdwa v99, v99, v98 dst_sel:DWORD dst_unused:UNUSED_PAD src0_sel:DWORD src1_sel:WORD_1
	v_or_b32_sdwa v98, v109, v108 dst_sel:DWORD dst_unused:UNUSED_PAD src0_sel:DWORD src1_sel:WORD_1
	v_and_b32_sdwa v108, v112, v185 dst_sel:DWORD dst_unused:UNUSED_PAD src0_sel:WORD_1 src1_sel:DWORD
	v_and_b32_sdwa v109, v106, v185 dst_sel:DWORD dst_unused:UNUSED_PAD src0_sel:WORD_1 src1_sel:DWORD
	v_add3_u32 v120, v106, v109, s43
	v_add3_u32 v121, v112, v108, s43
	v_and_b32_sdwa v108, v113, v185 dst_sel:DWORD dst_unused:UNUSED_PAD src0_sel:WORD_1 src1_sel:DWORD
	v_and_b32_sdwa v109, v107, v185 dst_sel:DWORD dst_unused:UNUSED_PAD src0_sel:WORD_1 src1_sel:DWORD
	v_add3_u32 v122, v113, v108, s43
	v_add3_u32 v123, v107, v109, s43
	v_mov_b32_e32 v108, v1
	v_mov_b32_e32 v109, v1
	v_cvt_pk_fp8_f32 v108, v100, v101
	v_cvt_pk_fp8_f32 v109, v106, v107
	v_and_b32_e32 v100, 0xffff0000, v122
	v_and_b32_e32 v106, 0xffff0000, v123
	v_cvt_pk_fp8_f32 v108, v104, v105 op_sel:[0,0,1]
	v_cvt_pk_fp8_f32 v109, v112, v113 op_sel:[0,0,1]
	v_or_b32_sdwa v101, v100, v121 dst_sel:DWORD dst_unused:UNUSED_PAD src0_sel:DWORD src1_sel:WORD_1
	v_or_b32_sdwa v100, v106, v120 dst_sel:DWORD dst_unused:UNUSED_PAD src0_sel:DWORD src1_sel:WORD_1
	global_store_dwordx2 v[102:103], v[126:127], off nt
	global_store_dwordx4 v[110:111], v[98:101], off offset:1024 nt
	global_store_dwordx2 v[102:103], v[108:109], off offset:512 nt
	v_lshl_add_u64 v[116:117], v[116:117], 0, s[54:55]
	s_waitcnt vmcnt(6)
	v_mov_b32_e32 v102, v54
	v_mov_b32_e32 v103, v55
	v_mov_b32_e32 v104, v56
	v_mov_b32_e32 v105, v57
	v_mov_b32_e32 v98, v50
	v_mov_b32_e32 v99, v51
	v_mov_b32_e32 v100, v52
	v_mov_b32_e32 v101, v53
	v_mov_b32_e32 v110, v38
	v_mov_b32_e32 v111, v39
	v_mov_b32_e32 v112, v40
	v_mov_b32_e32 v113, v41
	v_mov_b32_e32 v106, v34
	v_mov_b32_e32 v107, v35
	v_mov_b32_e32 v108, v36
	v_mov_b32_e32 v109, v37
	s_cbranch_scc0 .LBB0_758

; #define RP_UNPK(V_, H_) ((H_) ? (f32x4){bflo((V_)[2]), bfhi((V_)[2]), bflo((V_)[3]), bfhi((V_)[3])} : (f32x4){bflo((V_)[0]), bfhi((V_)[0]), bflo((V_)[1]), bfhi((V_)[1])})
; template <int MODE, bool FIRSTX>
; __device__ __forceinline__ void row_pass(Frame& F, int layer, bool final_out, int row0) {
;     ...
;         for (int q = 0; q < 4; ++q) v[q] = FIRSTX ? xf[q] : RP_UNPK(xb[q >> 1], q & 1);
;         if (MODE != 0) {
; #pragma unroll
;             for (int q = 0; q < 4; ++q) { f32x4 y = (f32x4){0.f, 0.f, 0.f, 0.f};
; #pragma unroll
;                 for (int k = 0; k < NY; ++k) { if (MODE == 2) { const unsigned w8 = yb[k][q >> 1][q & 1]; const f32x2 lo = __builtin_amdgcn_cvt_pk_f32_fp8((int)w8, false), hi = __builtin_amdgcn_cvt_pk_f32_fp8((int)w8, true); y += (f32x4){lo.x, lo.y, hi.x, hi.y}; }
;                                                 else y += RP_UNPK(yb[k][q >> 1], q & 1); }
;                 if (MODE == 2) y = y * (1.0f / YK8_SCALE);
;                 v[q] = v[q] * DN_ALPHA + gt[q] * y; }
;             float s = 0.f;
; #pragma unroll
;             for (int q = 0; q < 4; ++q) s += (v[q][0] + v[q][1]) + (v[q][2] + v[q][3]);
;             const float mean = wave_sum(s) * (1.0f / DM); float qq = 0.f;
; #pragma unroll
;             for (int q = 0; q < 4; ++q) { v[q] = v[q] - mean; qq += (v[q][0] * v[q][0] + v[q][1] * v[q][1]) + (v[q][2] * v[q][2] + v[q][3] * v[q][3]); }
;             const float rstd = 1.0f / sqrtf(wave_sum(qq) * (1.0f / DM) + LN_EPS);
.Lrp1f_common:
	v_lshlrev_b32_e32 v138, 16, v122
	v_and_b32_e32 v139, 0xffff0000, v122
	v_lshlrev_b32_e32 v122, 16, v123
	v_and_b32_e32 v123, 0xffff0000, v123
	v_pk_add_f32 v[122:123], v[122:123], 0 op_sel_hi:[1,0]
	v_pk_add_f32 v[138:139], v[138:139], 0 op_sel_hi:[1,0]
	v_pk_mul_f32 v[122:123], v[122:123], v[40:41]
	v_pk_mul_f32 v[138:139], v[138:139], v[38:39]
	v_pk_fma_f32 v[122:123], v[128:129], s[62:63], v[122:123] op_sel_hi:[1,0,1]
	v_lshlrev_b32_e32 v128, 16, v124
	v_and_b32_e32 v129, 0xffff0000, v124
	v_lshlrev_b32_e32 v124, 16, v125
	v_and_b32_e32 v125, 0xffff0000, v125
	v_pk_add_f32 v[124:125], v[124:125], 0 op_sel_hi:[1,0]
	v_pk_add_f32 v[128:129], v[128:129], 0 op_sel_hi:[1,0]
	v_pk_mul_f32 v[124:125], v[124:125], v[36:37]
	v_pk_fma_f32 v[126:127], v[126:127], s[62:63], v[138:139] op_sel_hi:[1,0,1]
	v_pk_fma_f32 v[120:121], v[120:121], s[62:63], v[124:125] op_sel_hi:[1,0,1]
	v_lshlrev_b32_e32 v124, 16, v114
	v_and_b32_e32 v125, 0xffff0000, v114
	v_lshlrev_b32_e32 v114, 16, v115
	v_and_b32_e32 v115, 0xffff0000, v115
	v_pk_add_f32 v[114:115], v[114:115], 0 op_sel_hi:[1,0]
	v_pk_mul_f32 v[128:129], v[128:129], v[34:35]
	v_pk_mul_f32 v[114:115], v[114:115], v[64:65]
	v_pk_fma_f32 v[118:119], v[118:119], s[62:63], v[128:129] op_sel_hi:[1,0,1]
	v_pk_fma_f32 v[112:113], v[112:113], s[62:63], v[114:115] op_sel_hi:[1,0,1]
	v_lshlrev_b32_e32 v114, 16, v116
	v_and_b32_e32 v115, 0xffff0000, v116
	v_lshlrev_b32_e32 v116, 16, v117
	v_and_b32_e32 v117, 0xffff0000, v117
	v_pk_add_f32 v[114:115], v[114:115], 0 op_sel_hi:[1,0]
	v_pk_add_f32 v[116:117], v[116:117], 0 op_sel_hi:[1,0]
	v_pk_mul_f32 v[114:115], v[114:115], v[54:55]
	v_pk_add_f32 v[124:125], v[124:125], 0 op_sel_hi:[1,0]
	v_pk_mul_f32 v[116:117], v[116:117], v[56:57]
	v_pk_fma_f32 v[106:107], v[106:107], s[62:63], v[114:115] op_sel_hi:[1,0,1]
	v_add_f32_e32 v114, v126, v127
	v_add_f32_e32 v115, v122, v123
	v_pk_mul_f32 v[124:125], v[124:125], v[62:63]
	v_pk_fma_f32 v[108:109], v[108:109], s[62:63], v[116:117] op_sel_hi:[1,0,1]
	v_add_f32_e32 v114, v114, v115
	v_add_f32_e32 v115, v118, v119
	v_add_f32_e32 v116, v120, v121
	v_pk_fma_f32 v[110:111], v[110:111], s[62:63], v[124:125] op_sel_hi:[1,0,1]
	v_add_f32_e32 v114, 0, v114
	v_add_f32_e32 v115, v115, v116
	v_add_f32_e32 v114, v115, v114
	v_add_f32_e32 v115, v110, v111
	v_add_f32_e32 v116, v112, v113
	v_add_f32_e32 v115, v115, v116
	v_add_f32_e32 v114, v115, v114
	v_add_f32_e32 v115, v106, v107
	v_add_f32_e32 v116, v108, v109
	v_add_f32_e32 v115, v115, v116
	v_add_f32_e32 v114, v115, v114
	ds_swizzle_b32 v115, v114 offset:swizzle(SWAP,1)
	s_add_u32 s76, s76, 1
	s_addc_u32 s77, s77, 0
	s_waitcnt lgkmcnt(0)
	v_add_f32_e32 v114, v114, v115
	ds_swizzle_b32 v115, v114 offset:swizzle(SWAP,2)
	s_waitcnt lgkmcnt(0)
	v_add_f32_e32 v114, v114, v115
	ds_swizzle_b32 v115, v114 offset:swizzle(SWAP,4)
	s_waitcnt lgkmcnt(0)
	v_add_f32_e32 v114, v114, v115
	ds_swizzle_b32 v115, v114 offset:swizzle(SWAP,8)
	s_waitcnt lgkmcnt(0)
	v_add_f32_e32 v114, v114, v115
	ds_swizzle_b32 v115, v114 offset:swizzle(SWAP,16)
	s_waitcnt lgkmcnt(0)
	v_add_f32_e32 v114, v114, v115
	v_mov_b32_e32 v115, v114
	s_nop 1
	v_permlane32_swap_b32_e32 v114, v115
	v_add_f32_e32 v114, v114, v115
	v_fmac_f32_e32 v123, 0xba800000, v114
	v_fmac_f32_e32 v127, 0xba800000, v114
	v_fmamk_f32 v122, v114, 0xba800000, v122
	v_fmamk_f32 v126, v114, 0xba800000, v126
	v_mul_f32_e32 v115, v127, v127
	v_mul_f32_e32 v116, v123, v123
	v_fmac_f32_e32 v115, v126, v126
	v_fmac_f32_e32 v116, v122, v122
	v_fmac_f32_e32 v121, 0xba800000, v114
	v_fmac_f32_e32 v119, 0xba800000, v114
	v_add_f32_e32 v115, v115, v116
	v_fmamk_f32 v120, v114, 0xba800000, v120
	v_fmamk_f32 v118, v114, 0xba800000, v118
	v_mul_f32_e32 v116, v119, v119
	v_mul_f32_e32 v117, v121, v121
	v_fmac_f32_e32 v116, v118, v118
	v_fmac_f32_e32 v117, v120, v120
	v_add_f32_e32 v116, v116, v117
	v_fmac_f32_e32 v113, 0xba800000, v114
	v_fmac_f32_e32 v111, 0xba800000, v114
	v_add_f32_e32 v115, v115, v116
	v_fmamk_f32 v112, v114, 0xba800000, v112
	v_fmamk_f32 v110, v114, 0xba800000, v110
	v_mul_f32_e32 v116, v111, v111
	v_mul_f32_e32 v117, v113, v113
	v_fmac_f32_e32 v116, v110, v110
	v_fmac_f32_e32 v117, v112, v112
	v_add_f32_e32 v116, v116, v117
	v_fmac_f32_e32 v109, 0xba800000, v114
	v_fmac_f32_e32 v107, 0xba800000, v114
	v_add_f32_e32 v115, v116, v115
	v_fmamk_f32 v108, v114, 0xba800000, v108
	v_fmamk_f32 v106, v114, 0xba800000, v106
	v_mul_f32_e32 v114, v107, v107
	v_mul_f32_e32 v116, v109, v109
	v_fmac_f32_e32 v114, v106, v106
	v_fmac_f32_e32 v116, v108, v108
	v_add_f32_e32 v114, v114, v116
	v_add_f32_e32 v114, v114, v115
	ds_swizzle_b32 v115, v114 offset:swizzle(SWAP,1)
	s_waitcnt lgkmcnt(0)
	v_add_f32_e32 v114, v114, v115
	ds_swizzle_b32 v115, v114 offset:swizzle(SWAP,2)
	s_waitcnt lgkmcnt(0)
	v_add_f32_e32 v114, v114, v115
	ds_swizzle_b32 v115, v114 offset:swizzle(SWAP,4)
	s_waitcnt lgkmcnt(0)
	v_add_f32_e32 v114, v114, v115
	ds_swizzle_b32 v115, v114 offset:swizzle(SWAP,8)
	s_waitcnt lgkmcnt(0)
	v_add_f32_e32 v114, v114, v115
	ds_swizzle_b32 v115, v114 offset:swizzle(SWAP,16)
	s_waitcnt lgkmcnt(0)
; __device__ __forceinline__ unsigned pk2(float lo, float hi) { return f2bf(lo) | (f2bf(hi) << 16); }
; template <int MODE, bool FIRSTX>
; __device__ __forceinline__ void row_pass(Frame& F, int layer, bool final_out, int row0) {
;     ...
;             const float rstd = 1.0f / sqrtf(wave_sum(qq) * (1.0f / DM) + LN_EPS);
; #pragma unroll
;             for (int q = 0; q < 4; ++q) v[q] = v[q] * rstd * lg[q] + lb[q];
;             if (final_out) { if (row >= NCTX) {
; #pragma unroll
;                 for (int q = 0; q < 4; ++q) *(f32x4*)(F.out + (size_t)(row - NCTX) * DM + RP_COL(q)) = v[q]; } }
;             else {
; #pragma unroll
;                 for (int j = 0; j < 2; ++j) { u32x4 w; w.x = pk2(v[2 * j][0], v[2 * j][1]); w.y = pk2(v[2 * j][2], v[2 * j][3]); w.z = pk2(v[2 * j + 1][0], v[2 * j + 1][1]); w.w = pk2(v[2 * j + 1][2], v[2 * j + 1][3]);
;                     *(u32x4*)(X + (size_t)row * DM + lc + 512 * j) = w; } }
;         }
;         if (!final_out) {
; #pragma unroll
;             for (int j = 0; j < 2; ++j) { const f32x4 h0 = v[2 * j] * (sc[2 * j] + 1.0f) + sh[2 * j], h1 = v[2 * j + 1] * (sc[2 * j + 1] + 1.0f) + sh[2 * j + 1];
;                 if (MODE == 1 || (nlayer % 3) == 2) { u32x4 w; w.x = pk2(h0[0], h0[1]); w.y = pk2(h0[2], h0[3]); w.z = pk2(h1[0], h1[1]); w.w = pk2(h1[2], h1[3]);
;                     *(u32x4*)(H + (size_t)row * DM + lc + 512 * j) = w; }
	v_add_f32_e32 v114, v114, v115
	v_mov_b32_e32 v115, v114
	s_nop 1
	v_permlane32_swap_b32_e32 v114, v115
	v_add_f32_e32 v114, v114, v115
	v_fmamk_f32 v114, v114, 0x3a800000, v188
	v_mul_f32_e32 v115, 0x4f800000, v114
	v_cmp_gt_f32_e32 vcc, s31, v114
	s_nop 1
	v_cndmask_b32_e32 v114, v114, v115, vcc
	v_sqrt_f32_e32 v115, v114
	s_nop 0
	v_add_u32_e32 v116, -1, v115
	v_fma_f32 v117, -v116, v115, v114
	v_cmp_ge_f32_e64 s[2:3], 0, v117
	v_add_u32_e32 v117, 1, v115
	s_nop 0
	v_cndmask_b32_e64 v116, v115, v116, s[2:3]
	v_fma_f32 v115, -v117, v115, v114
	v_cmp_lt_f32_e64 s[2:3], 0, v115
	s_nop 1
	v_cndmask_b32_e64 v115, v116, v117, s[2:3]
	v_mul_f32_e32 v116, 0x37800000, v115
	v_cndmask_b32_e32 v115, v115, v116, vcc
	v_cmp_class_f32_e32 vcc, v114, v189
	s_nop 1
	v_cndmask_b32_e32 v114, v115, v114, vcc
	v_div_scale_f32 v115, s[0:1], v114, v114, 1.0
	v_rcp_f32_e32 v116, v115
	s_add_i32 s0, s4, s76
	s_add_u32 s60, s60, 0x1000
	s_addc_u32 s61, s61, 0
	v_fma_f32 v117, -v115, v116, 1.0
	v_fmac_f32_e32 v116, v117, v116
	v_div_scale_f32 v117, vcc, 1.0, v114, 1.0
	v_mul_f32_e32 v124, v117, v116
	v_fma_f32 v125, -v115, v124, v117
	v_fmac_f32_e32 v124, v125, v116
	v_fma_f32 v115, -v115, v124, v117
	v_div_fmas_f32 v115, v115, v116, v124
	v_div_fixup_f32 v114, v115, v114, 1.0
	v_pk_mul_f32 v[116:117], v[126:127], v[114:115] op_sel_hi:[1,0]
	v_pk_mul_f32 v[106:107], v[106:107], v[114:115] op_sel_hi:[1,0]
	v_pk_fma_f32 v[116:117], v[2:3], v[116:117], v[6:7]
	v_pk_mul_f32 v[122:123], v[122:123], v[114:115] op_sel_hi:[1,0]
	v_pk_mul_f32 v[118:119], v[118:119], v[114:115] op_sel_hi:[1,0]
	v_pk_mul_f32 v[120:121], v[120:121], v[114:115] op_sel_hi:[1,0]
	v_pk_mul_f32 v[110:111], v[110:111], v[114:115] op_sel_hi:[1,0]
	v_pk_mul_f32 v[112:113], v[112:113], v[114:115] op_sel_hi:[1,0]
	v_pk_mul_f32 v[108:109], v[108:109], v[114:115] op_sel_hi:[1,0]
	v_pk_fma_f32 v[114:115], v[26:27], v[106:107], v[30:31]
	v_bfe_u32 v106, v116, 16, 1
	v_add3_u32 v106, v116, v106, s43
	v_bfe_u32 v107, v117, 16, 1
	v_pk_fma_f32 v[122:123], v[4:5], v[122:123], v[8:9]
	v_lshrrev_b32_e32 v106, 16, v106
	v_add3_u32 v107, v117, v107, s43
	v_and_or_b32 v106, v107, s33, v106
	v_bfe_u32 v107, v122, 16, 1
	v_pk_fma_f32 v[124:125], v[28:29], v[108:109], v[32:33]
	v_add3_u32 v107, v122, v107, s43
	v_bfe_u32 v108, v123, 16, 1
	v_pk_fma_f32 v[118:119], v[10:11], v[118:119], v[14:15]
	v_lshrrev_b32_e32 v107, 16, v107
	v_add3_u32 v108, v123, v108, s43
	v_and_or_b32 v107, v108, s33, v107
	v_bfe_u32 v108, v118, 16, 1
	v_add3_u32 v108, v118, v108, s43
	v_bfe_u32 v109, v119, 16, 1
	v_pk_fma_f32 v[120:121], v[12:13], v[120:121], v[16:17]
	v_lshrrev_b32_e32 v108, 16, v108
	v_add3_u32 v109, v119, v109, s43
	v_and_or_b32 v108, v109, s33, v108
	v_bfe_u32 v109, v120, 16, 1
	v_add3_u32 v109, v120, v109, s43
	v_bfe_u32 v128, v121, 16, 1
	v_lshl_add_u64 v[126:127], s[74:75], 0, v[132:133]
	v_lshrrev_b32_e32 v109, 16, v109
	v_add3_u32 v128, v121, v128, s43
	v_and_or_b32 v109, v128, s33, v109
	v_add_co_u32_e32 v128, vcc, s39, v126
	v_pk_fma_f32 v[110:111], v[18:19], v[110:111], v[22:23]
	s_nop 0
	v_addc_co_u32_e32 v129, vcc, 0, v127, vcc
	global_store_dwordx4 v[128:129], v[106:109], off nt
	v_pk_fma_f32 v[112:113], v[20:21], v[112:113], v[24:25]
	v_bfe_u32 v137, v125, 16, 1
	v_bfe_u32 v106, v110, 16, 1
	v_add3_u32 v106, v110, v106, s43
	v_bfe_u32 v107, v111, 16, 1
	v_lshrrev_b32_e32 v106, 16, v106
	v_add3_u32 v107, v111, v107, s43
	v_and_or_b32 v106, v107, s33, v106
	v_bfe_u32 v107, v112, 16, 1
	v_add3_u32 v107, v112, v107, s43
	v_bfe_u32 v108, v113, 16, 1
	v_lshrrev_b32_e32 v107, 16, v107
	v_add3_u32 v108, v113, v108, s43
	v_and_or_b32 v107, v108, s33, v107
	v_bfe_u32 v108, v114, 16, 1
	v_add3_u32 v108, v114, v108, s43
	v_bfe_u32 v109, v115, 16, 1
	v_lshrrev_b32_e32 v108, 16, v108
	v_add3_u32 v109, v115, v109, s43
	v_and_or_b32 v108, v109, s33, v108
	v_bfe_u32 v109, v124, 16, 1
	v_add3_u32 v109, v124, v109, s43
	v_lshrrev_b32_e32 v109, 16, v109
	v_add3_u32 v137, v125, v137, s43
	v_and_or_b32 v109, v137, s33, v109
	global_store_dwordx4 v[128:129], v[106:109], off offset:1024 nt
	v_lshl_add_u64 v[132:133], v[132:133], 0, s[50:51]
	s_cmp_ge_i32 s0, s11
	v_pk_add_f32 v[106:107], v[60:61], 1.0 op_sel_hi:[1,0]
	v_pk_add_f32 v[108:109], v[58:59], 1.0 op_sel_hi:[1,0]
	v_pk_fma_f32 v[122:123], v[106:107], v[122:123], v[48:49]
	v_pk_fma_f32 v[116:117], v[108:109], v[116:117], v[46:47]
	v_pk_add_f32 v[106:107], v[52:53], 1.0 op_sel_hi:[1,0]
	v_pk_add_f32 v[108:109], v[50:51], 1.0 op_sel_hi:[1,0]
	v_pk_fma_f32 v[120:121], v[106:107], v[120:121], v[44:45]
	v_and_b32_sdwa v107, v116, v185 dst_sel:DWORD dst_unused:UNUSED_PAD src0_sel:WORD_1 src1_sel:DWORD
	v_pk_fma_f32 v[118:119], v[108:109], v[118:119], v[42:43]
	v_add3_u32 v108, v116, v107, s43
	v_and_b32_sdwa v107, v123, v185 dst_sel:DWORD dst_unused:UNUSED_PAD src0_sel:WORD_1 src1_sel:DWORD
	v_and_b32_sdwa v109, v117, v185 dst_sel:DWORD dst_unused:UNUSED_PAD src0_sel:WORD_1 src1_sel:DWORD
; __device__ __forceinline__ unsigned pk2(float lo, float hi) { return f2bf(lo) | (f2bf(hi) << 16); }
; __device__ __forceinline__ unsigned cvt_fp8x4(float a, float b, float c, float d) { int w = __builtin_amdgcn_cvt_pk_fp8_f32(a, b, 0, false); w = __builtin_amdgcn_cvt_pk_fp8_f32(c, d, w, true); return (unsigned)w; }
; template <int MODE, bool FIRSTX>
; __device__ __forceinline__ void row_pass(Frame& F, int layer, bool final_out, int row0) {
;     ...
;         if (!final_out) {
; #pragma unroll
;             for (int j = 0; j < 2; ++j) { const f32x4 h0 = v[2 * j] * (sc[2 * j] + 1.0f) + sh[2 * j], h1 = v[2 * j + 1] * (sc[2 * j + 1] + 1.0f) + sh[2 * j + 1];
;                 if (MODE == 1 || (nlayer % 3) == 2) { u32x4 w; w.x = pk2(h0[0], h0[1]); w.y = pk2(h0[2], h0[3]); w.z = pk2(h1[0], h1[1]); w.w = pk2(h1[2], h1[3]);
;                     *(u32x4*)(H + (size_t)row * DM + lc + 512 * j) = w; }
;                 if (MODE == 1 || (nlayer % 3) != 2) {                                u32x2 w8; w8.x = cvt_fp8x4(h0[0], h0[1], h0[2], h0[3]); w8.y = cvt_fp8x4(h1[0], h1[1], h1[2], h1[3]); *(u32x2*)(F.ws + WS_H8 + (size_t)row * DM + lc + 512 * j) = w8; } }
;         }
; #pragma unroll
;         for (int q = 0; q < 4; ++q) xf[q] = xfn[q];
; #pragma unroll
;         for (int j = 0; j < 2; ++j) { xb[j] = xbn[j];
; #pragma unroll
;             for (int k = 0; k < (NY ? NY : 1); ++k) yb[k][j] = ybn[k][j]; }
	v_and_b32_sdwa v106, v122, v185 dst_sel:DWORD dst_unused:UNUSED_PAD src0_sel:WORD_1 src1_sel:DWORD
	v_add3_u32 v107, v123, v107, s43
	v_add3_u32 v109, v117, v109, s43
	v_add3_u32 v106, v122, v106, s43
	v_and_b32_e32 v107, 0xffff0000, v107
	v_and_b32_e32 v109, 0xffff0000, v109
	v_or_b32_sdwa v107, v107, v106 dst_sel:DWORD dst_unused:UNUSED_PAD src0_sel:DWORD src1_sel:WORD_1
	v_or_b32_sdwa v106, v109, v108 dst_sel:DWORD dst_unused:UNUSED_PAD src0_sel:DWORD src1_sel:WORD_1
	v_and_b32_sdwa v109, v118, v185 dst_sel:DWORD dst_unused:UNUSED_PAD src0_sel:WORD_1 src1_sel:DWORD
	v_add3_u32 v128, v118, v109, s43
	v_and_b32_sdwa v109, v121, v185 dst_sel:DWORD dst_unused:UNUSED_PAD src0_sel:WORD_1 src1_sel:DWORD
	v_and_b32_sdwa v129, v119, v185 dst_sel:DWORD dst_unused:UNUSED_PAD src0_sel:WORD_1 src1_sel:DWORD
	v_and_b32_sdwa v108, v120, v185 dst_sel:DWORD dst_unused:UNUSED_PAD src0_sel:WORD_1 src1_sel:DWORD
	v_add3_u32 v109, v121, v109, s43
	v_add3_u32 v129, v119, v129, s43
	v_add3_u32 v108, v120, v108, s43
	v_and_b32_e32 v109, 0xffff0000, v109
	v_and_b32_e32 v129, 0xffff0000, v129
	v_or_b32_sdwa v109, v109, v108 dst_sel:DWORD dst_unused:UNUSED_PAD src0_sel:DWORD src1_sel:WORD_1
	v_or_b32_sdwa v108, v129, v128 dst_sel:DWORD dst_unused:UNUSED_PAD src0_sel:DWORD src1_sel:WORD_1
	v_mov_b32_e32 v128, v1
	v_cvt_pk_fp8_f32 v128, v116, v117
	v_add_co_u32_e32 v116, vcc, s28, v126
	v_mov_b32_e32 v129, v1
	s_nop 0
	v_addc_co_u32_e32 v117, vcc, 0, v127, vcc
	v_cvt_pk_fp8_f32 v129, v118, v119
	global_store_dwordx4 v[116:117], v[106:109], off nt
	v_cvt_pk_fp8_f32 v128, v122, v123 op_sel:[0,0,1]
	v_cvt_pk_fp8_f32 v129, v120, v121 op_sel:[0,0,1]
	v_lshl_add_u64 v[106:107], s[74:75], 0, v[134:135]
	v_add_co_u32_e32 v118, vcc, s38, v106
	v_pk_add_f32 v[108:109], v[78:79], 1.0 op_sel_hi:[1,0]
	s_nop 0
	v_addc_co_u32_e32 v119, vcc, 0, v107, vcc
	v_pk_add_f32 v[106:107], v[80:81], 1.0 op_sel_hi:[1,0]
	v_pk_fma_f32 v[108:109], v[108:109], v[110:111], v[70:71]
	v_pk_fma_f32 v[112:113], v[106:107], v[112:113], v[72:73]
	v_pk_add_f32 v[106:107], v[76:77], 1.0 op_sel_hi:[1,0]
	v_pk_add_f32 v[110:111], v[74:75], 1.0 op_sel_hi:[1,0]
	v_pk_fma_f32 v[120:121], v[106:107], v[124:125], v[68:69]
	v_and_b32_sdwa v107, v108, v185 dst_sel:DWORD dst_unused:UNUSED_PAD src0_sel:WORD_1 src1_sel:DWORD
	v_pk_fma_f32 v[110:111], v[110:111], v[114:115], v[66:67]
	v_add3_u32 v114, v108, v107, s43
	v_and_b32_sdwa v107, v113, v185 dst_sel:DWORD dst_unused:UNUSED_PAD src0_sel:WORD_1 src1_sel:DWORD
	v_and_b32_sdwa v115, v109, v185 dst_sel:DWORD dst_unused:UNUSED_PAD src0_sel:WORD_1 src1_sel:DWORD
	v_and_b32_sdwa v106, v112, v185 dst_sel:DWORD dst_unused:UNUSED_PAD src0_sel:WORD_1 src1_sel:DWORD
	v_add3_u32 v107, v113, v107, s43
	v_add3_u32 v115, v109, v115, s43
	v_add3_u32 v106, v112, v106, s43
	v_and_b32_e32 v107, 0xffff0000, v107
	v_and_b32_e32 v115, 0xffff0000, v115
	v_or_b32_sdwa v107, v107, v106 dst_sel:DWORD dst_unused:UNUSED_PAD src0_sel:DWORD src1_sel:WORD_1
	v_or_b32_sdwa v106, v115, v114 dst_sel:DWORD dst_unused:UNUSED_PAD src0_sel:DWORD src1_sel:WORD_1
	v_and_b32_sdwa v114, v120, v185 dst_sel:DWORD dst_unused:UNUSED_PAD src0_sel:WORD_1 src1_sel:DWORD
	v_and_b32_sdwa v115, v110, v185 dst_sel:DWORD dst_unused:UNUSED_PAD src0_sel:WORD_1 src1_sel:DWORD
	v_add3_u32 v122, v110, v115, s43
	v_add3_u32 v123, v120, v114, s43
	v_and_b32_sdwa v114, v121, v185 dst_sel:DWORD dst_unused:UNUSED_PAD src0_sel:WORD_1 src1_sel:DWORD
	v_and_b32_sdwa v115, v111, v185 dst_sel:DWORD dst_unused:UNUSED_PAD src0_sel:WORD_1 src1_sel:DWORD
	v_add3_u32 v124, v121, v114, s43
	v_add3_u32 v125, v111, v115, s43
	v_mov_b32_e32 v114, v1
	v_mov_b32_e32 v115, v1
	v_cvt_pk_fp8_f32 v114, v108, v109
	v_cvt_pk_fp8_f32 v115, v110, v111
	v_and_b32_e32 v108, 0xffff0000, v124
	v_and_b32_e32 v110, 0xffff0000, v125
	v_cvt_pk_fp8_f32 v114, v112, v113 op_sel:[0,0,1]
	v_cvt_pk_fp8_f32 v115, v120, v121 op_sel:[0,0,1]
	v_or_b32_sdwa v109, v108, v123 dst_sel:DWORD dst_unused:UNUSED_PAD src0_sel:DWORD src1_sel:WORD_1
	v_or_b32_sdwa v108, v110, v122 dst_sel:DWORD dst_unused:UNUSED_PAD src0_sel:DWORD src1_sel:WORD_1
	global_store_dwordx2 v[118:119], v[128:129], off nt
	global_store_dwordx4 v[116:117], v[106:109], off offset:1024 nt
	global_store_dwordx2 v[118:119], v[114:115], off offset:512 nt
	s_waitcnt vmcnt(6)
	v_mov_b64_e32 v[112:113], v[96:97]
	v_mov_b64_e32 v[108:109], v[92:93]
	v_mov_b64_e32 v[120:121], v[84:85]
	v_mov_b64_e32 v[128:129], v[88:89]
	v_lshl_add_u64 v[134:135], v[134:135], 0, s[54:55]
	v_mov_b64_e32 v[106:107], v[90:91]
	v_mov_b64_e32 v[110:111], v[94:95]
	v_mov_b64_e32 v[118:119], v[82:83]
	v_mov_b64_e32 v[126:127], v[86:87]
	v_mov_b32_e32 v122, v98
	v_mov_b32_e32 v123, v99
	v_mov_b32_e32 v124, v100
	v_mov_b32_e32 v125, v101
	v_mov_b32_e32 v114, v102
	v_mov_b32_e32 v115, v103
	v_mov_b32_e32 v116, v104
	v_mov_b32_e32 v117, v105
	s_cbranch_scc1 .LBB0_777

; #define RP_UNPK(V_, H_) ((H_) ? (f32x4){bflo((V_)[2]), bfhi((V_)[2]), bflo((V_)[3]), bfhi((V_)[3])} : (f32x4){bflo((V_)[0]), bfhi((V_)[0]), bflo((V_)[1]), bfhi((V_)[1])})
; template <int MODE, bool FIRSTX>
; __device__ __forceinline__ void row_pass(Frame& F, int layer, bool final_out, int row0) {
;     ...
;         for (int q = 0; q < 4; ++q) v[q] = FIRSTX ? xf[q] : RP_UNPK(xb[q >> 1], q & 1);
;         if (MODE != 0) {
; #pragma unroll
;             for (int q = 0; q < 4; ++q) { f32x4 y = (f32x4){0.f, 0.f, 0.f, 0.f};
; #pragma unroll
;                 for (int k = 0; k < NY; ++k) { if (MODE == 2) { const unsigned w8 = yb[k][q >> 1][q & 1]; const f32x2 lo = __builtin_amdgcn_cvt_pk_f32_fp8((int)w8, false), hi = __builtin_amdgcn_cvt_pk_f32_fp8((int)w8, true); y += (f32x4){lo.x, lo.y, hi.x, hi.y}; }
;                                                 else y += RP_UNPK(yb[k][q >> 1], q & 1); }
;                 if (MODE == 2) y = y * (1.0f / YK8_SCALE);
;                 v[q] = v[q] * DN_ALPHA + gt[q] * y; }
;             float s = 0.f;
; #pragma unroll
;             for (int q = 0; q < 4; ++q) s += (v[q][0] + v[q][1]) + (v[q][2] + v[q][3]);
;             const float mean = wave_sum(s) * (1.0f / DM); float qq = 0.f;
.LBB0_1210:
	v_lshlrev_b32_e32 v154, 16, v96
	v_and_b32_e32 v155, 0xffff0000, v96
	v_lshlrev_b32_e32 v156, 16, v97
	v_and_b32_e32 v157, 0xffff0000, v97
	v_lshlrev_b32_e32 v158, 16, v90
	v_and_b32_e32 v159, 0xffff0000, v90
	v_lshlrev_b32_e32 v160, 16, v91
	v_and_b32_e32 v161, 0xffff0000, v91
	v_lshlrev_b32_e32 v96, 16, v92
	v_and_b32_e32 v97, 0xffff0000, v92
	v_lshlrev_b32_e32 v150, 16, v93
	v_and_b32_e32 v151, 0xffff0000, v93
	v_cvt_pk_f32_fp8_e32 v[90:91], v142
	v_cvt_pk_f32_fp8_sdwa v[92:93], v142 src0_sel:WORD_1
	v_cvt_pk_f32_fp8_e32 v[162:163], v140
	v_cvt_pk_f32_fp8_sdwa v[164:165], v140 src0_sel:WORD_1
	v_pk_add_f32 v[90:91], v[90:91], 0 op_sel_hi:[1,0]
	v_pk_add_f32 v[92:93], v[92:93], 0 op_sel_hi:[1,0]
	v_pk_add_f32 v[90:91], v[90:91], v[162:163]
	v_pk_add_f32 v[92:93], v[92:93], v[164:165]
	v_cvt_pk_f32_fp8_e32 v[162:163], v144
	v_cvt_pk_f32_fp8_sdwa v[164:165], v144 src0_sel:WORD_1
	v_lshlrev_b32_e32 v152, 16, v94
	v_and_b32_e32 v153, 0xffff0000, v94
	v_pk_add_f32 v[90:91], v[90:91], v[162:163]
	v_pk_add_f32 v[92:93], v[92:93], v[164:165]
	v_cvt_pk_f32_fp8_e32 v[162:163], v148
	v_cvt_pk_f32_fp8_sdwa v[164:165], v148 src0_sel:WORD_1
	v_lshlrev_b32_e32 v94, 16, v95
	v_and_b32_e32 v95, 0xffff0000, v95
	v_pk_add_f32 v[90:91], v[90:91], v[162:163]
	v_pk_add_f32 v[92:93], v[92:93], v[164:165]
	v_pk_mul_f32 v[90:91], v[90:91], s[70:71] op_sel_hi:[1,0]
	v_pk_mul_f32 v[92:93], v[92:93], s[70:71] op_sel_hi:[1,0]
	v_pk_mul_f32 v[162:163], v[70:71], v[90:91]
	v_pk_mul_f32 v[90:91], v[72:73], v[92:93]
	v_pk_fma_f32 v[92:93], v[152:153], s[62:63], v[162:163] op_sel_hi:[1,0,1]
	v_pk_fma_f32 v[90:91], v[94:95], s[62:63], v[90:91] op_sel_hi:[1,0,1]
	v_cvt_pk_f32_fp8_e32 v[94:95], v143
	v_cvt_pk_f32_fp8_sdwa v[142:143], v143 src0_sel:WORD_1
	v_cvt_pk_f32_fp8_e32 v[152:153], v141
	v_cvt_pk_f32_fp8_sdwa v[140:141], v141 src0_sel:WORD_1
	v_pk_add_f32 v[94:95], v[94:95], 0 op_sel_hi:[1,0]
	v_pk_add_f32 v[142:143], v[142:143], 0 op_sel_hi:[1,0]
	v_pk_add_f32 v[94:95], v[94:95], v[152:153]
	v_pk_add_f32 v[140:141], v[142:143], v[140:141]
	v_cvt_pk_f32_fp8_e32 v[142:143], v145
	v_cvt_pk_f32_fp8_sdwa v[144:145], v145 src0_sel:WORD_1
	v_cvt_pk_f32_fp8_sdwa v[152:153], v98 src0_sel:WORD_1
	v_add_f32_e32 v0, v92, v93
	v_pk_add_f32 v[94:95], v[94:95], v[142:143]
	v_cvt_pk_f32_fp8_e32 v[142:143], v149
	v_pk_add_f32 v[140:141], v[140:141], v[144:145]
	v_cvt_pk_f32_fp8_sdwa v[144:145], v149 src0_sel:WORD_1
	v_cvt_pk_f32_fp8_e32 v[148:149], v98
	v_pk_add_f32 v[94:95], v[94:95], v[142:143]
	v_pk_add_f32 v[140:141], v[140:141], v[144:145]
	v_pk_mul_f32 v[94:95], v[94:95], s[70:71] op_sel_hi:[1,0]
	v_pk_mul_f32 v[140:141], v[140:141], s[70:71] op_sel_hi:[1,0]
	v_pk_mul_f32 v[142:143], v[74:75], v[94:95]
	v_pk_mul_f32 v[94:95], v[76:77], v[140:141]
	v_pk_fma_f32 v[140:141], v[154:155], s[62:63], v[142:143] op_sel_hi:[1,0,1]
	v_cvt_pk_f32_fp8_e32 v[142:143], v100
	v_cvt_pk_f32_fp8_sdwa v[144:145], v100 src0_sel:WORD_1
	v_pk_fma_f32 v[94:95], v[156:157], s[62:63], v[94:95] op_sel_hi:[1,0,1]
	v_pk_add_f32 v[142:143], v[142:143], 0 op_sel_hi:[1,0]
	v_pk_add_f32 v[144:145], v[144:145], 0 op_sel_hi:[1,0]
	v_pk_add_f32 v[142:143], v[142:143], v[148:149]
	v_cvt_pk_f32_fp8_e32 v[148:149], v102
	v_pk_add_f32 v[144:145], v[144:145], v[152:153]
	v_cvt_pk_f32_fp8_sdwa v[152:153], v102 src0_sel:WORD_1
	v_pk_add_f32 v[142:143], v[142:143], v[148:149]
	v_cvt_pk_f32_fp8_e32 v[148:149], v104
	v_pk_add_f32 v[144:145], v[144:145], v[152:153]
	v_cvt_pk_f32_fp8_sdwa v[152:153], v104 src0_sel:WORD_1
	v_pk_add_f32 v[142:143], v[142:143], v[148:149]
	v_cvt_pk_f32_fp8_e32 v[148:149], v101
	v_cvt_pk_f32_fp8_sdwa v[100:101], v101 src0_sel:WORD_1
	v_pk_add_f32 v[144:145], v[144:145], v[152:153]
	v_cvt_pk_f32_fp8_e32 v[152:153], v99
	v_cvt_pk_f32_fp8_sdwa v[98:99], v99 src0_sel:WORD_1
	v_pk_add_f32 v[100:101], v[100:101], 0 op_sel_hi:[1,0]
	v_pk_add_f32 v[148:149], v[148:149], 0 op_sel_hi:[1,0]
	v_pk_mul_f32 v[144:145], v[144:145], s[70:71] op_sel_hi:[1,0]
	v_pk_add_f32 v[98:99], v[100:101], v[98:99]
	v_cvt_pk_f32_fp8_e32 v[100:101], v103
	v_cvt_pk_f32_fp8_sdwa v[102:103], v103 src0_sel:WORD_1
	v_pk_add_f32 v[148:149], v[148:149], v[152:153]
	v_pk_mul_f32 v[142:143], v[142:143], s[70:71] op_sel_hi:[1,0]
	v_pk_add_f32 v[100:101], v[148:149], v[100:101]
	v_pk_add_f32 v[98:99], v[98:99], v[102:103]
	v_cvt_pk_f32_fp8_e32 v[102:103], v105
	v_cvt_pk_f32_fp8_sdwa v[104:105], v105 src0_sel:WORD_1
	v_pk_mul_f32 v[142:143], v[78:79], v[142:143]
	v_pk_mul_f32 v[144:145], v[80:81], v[144:145]
	v_pk_add_f32 v[100:101], v[100:101], v[102:103]
	v_pk_add_f32 v[98:99], v[98:99], v[104:105]
	v_pk_fma_f32 v[144:145], v[160:161], s[62:63], v[144:145] op_sel_hi:[1,0,1]
	v_pk_mul_f32 v[98:99], v[98:99], s[70:71] op_sel_hi:[1,0]
	v_pk_fma_f32 v[142:143], v[158:159], s[62:63], v[142:143] op_sel_hi:[1,0,1]
	v_pk_mul_f32 v[98:99], v[88:89], v[98:99]
	v_pk_mul_f32 v[100:101], v[100:101], s[70:71] op_sel_hi:[1,0]
	v_pk_fma_f32 v[148:149], v[150:151], s[62:63], v[98:99] op_sel_hi:[1,0,1]
	v_add_f32_e32 v98, v90, v91
	v_add_f32_e32 v0, v0, v98
	v_add_f32_e32 v98, v140, v141
	v_add_f32_e32 v99, v94, v95
	v_add_f32_e32 v0, 0, v0
	v_add_f32_e32 v98, v98, v99
	v_pk_mul_f32 v[100:101], v[86:87], v[100:101]
	v_add_f32_e32 v0, v0, v98
	v_add_f32_e32 v98, v142, v143
	v_add_f32_e32 v99, v144, v145
	v_pk_fma_f32 v[96:97], v[96:97], s[62:63], v[100:101] op_sel_hi:[1,0,1]
	v_add_f32_e32 v98, v98, v99
	v_add_f32_e32 v0, v0, v98
	v_add_f32_e32 v98, v96, v97
	v_add_f32_e32 v99, v148, v149
	v_add_f32_e32 v98, v98, v99
	v_add_f32_e32 v0, v0, v98
	ds_swizzle_b32 v98, v0 offset:swizzle(SWAP,1)
	s_waitcnt lgkmcnt(0)
; __device__ __forceinline__ unsigned pk2(float lo, float hi) { return f2bf(lo) | (f2bf(hi) << 16); }
; template <int MODE, bool FIRSTX>
; __device__ __forceinline__ void row_pass(Frame& F, int layer, bool final_out, int row0) {
;     ...
;             float s = 0.f;
; #pragma unroll
;             for (int q = 0; q < 4; ++q) s += (v[q][0] + v[q][1]) + (v[q][2] + v[q][3]);
;             const float mean = wave_sum(s) * (1.0f / DM); float qq = 0.f;
; #pragma unroll
;             for (int q = 0; q < 4; ++q) { v[q] = v[q] - mean; qq += (v[q][0] * v[q][0] + v[q][1] * v[q][1]) + (v[q][2] * v[q][2] + v[q][3] * v[q][3]); }
;             const float rstd = 1.0f / sqrtf(wave_sum(qq) * (1.0f / DM) + LN_EPS);
; #pragma unroll
;             for (int q = 0; q < 4; ++q) v[q] = v[q] * rstd * lg[q] + lb[q];
;             if (final_out) { if (row >= NCTX) {
; #pragma unroll
;                 for (int q = 0; q < 4; ++q) *(f32x4*)(F.out + (size_t)(row - NCTX) * DM + RP_COL(q)) = v[q]; } }
;             else {
; #pragma unroll
;                 for (int j = 0; j < 2; ++j) { u32x4 w; w.x = pk2(v[2 * j][0], v[2 * j][1]); w.y = pk2(v[2 * j][2], v[2 * j][3]); w.z = pk2(v[2 * j + 1][0], v[2 * j + 1][1]); w.w = pk2(v[2 * j + 1][2], v[2 * j + 1][3]);
;                     *(u32x4*)(X + (size_t)row * DM + lc + 512 * j) = w; } }
	v_add_f32_e32 v0, v0, v98
	ds_swizzle_b32 v98, v0 offset:swizzle(SWAP,2)
	s_waitcnt lgkmcnt(0)
	v_add_f32_e32 v0, v0, v98
	ds_swizzle_b32 v98, v0 offset:swizzle(SWAP,4)
	s_waitcnt lgkmcnt(0)
	v_add_f32_e32 v0, v0, v98
	ds_swizzle_b32 v98, v0 offset:swizzle(SWAP,8)
	s_waitcnt lgkmcnt(0)
	v_add_f32_e32 v0, v0, v98
	ds_swizzle_b32 v98, v0 offset:swizzle(SWAP,16)
	s_waitcnt lgkmcnt(0)
	v_add_f32_e32 v0, v0, v98
	v_mov_b32_e32 v98, v0
	s_nop 1
	v_permlane32_swap_b32_e32 v0, v98
	v_add_f32_e32 v0, v0, v98
	v_fmac_f32_e32 v91, 0xba800000, v0
	v_fmac_f32_e32 v93, 0xba800000, v0
	v_fmamk_f32 v90, v0, 0xba800000, v90
	v_fmamk_f32 v92, v0, 0xba800000, v92
	v_mul_f32_e32 v98, v93, v93
	v_mul_f32_e32 v99, v91, v91
	v_fmac_f32_e32 v98, v92, v92
	v_fmac_f32_e32 v99, v90, v90
	v_fmac_f32_e32 v95, 0xba800000, v0
	v_fmac_f32_e32 v141, 0xba800000, v0
	v_add_f32_e32 v98, v98, v99
	v_fmamk_f32 v94, v0, 0xba800000, v94
	v_fmamk_f32 v140, v0, 0xba800000, v140
	v_mul_f32_e32 v99, v141, v141
	v_mul_f32_e32 v100, v95, v95
	v_fmac_f32_e32 v99, v140, v140
	v_fmac_f32_e32 v100, v94, v94
	v_add_f32_e32 v99, v99, v100
	v_fmac_f32_e32 v145, 0xba800000, v0
	v_fmac_f32_e32 v143, 0xba800000, v0
	v_add_f32_e32 v98, v98, v99
	v_fmamk_f32 v144, v0, 0xba800000, v144
	v_fmamk_f32 v142, v0, 0xba800000, v142
	v_mul_f32_e32 v99, v143, v143
	v_mul_f32_e32 v100, v145, v145
	v_fmac_f32_e32 v99, v142, v142
	v_fmac_f32_e32 v100, v144, v144
	v_add_f32_e32 v99, v99, v100
	v_fmac_f32_e32 v149, 0xba800000, v0
	v_fmac_f32_e32 v97, 0xba800000, v0
	v_add_f32_e32 v98, v99, v98
	v_fmamk_f32 v148, v0, 0xba800000, v148
	v_fmamk_f32 v96, v0, 0xba800000, v96
	v_mul_f32_e32 v0, v97, v97
	v_mul_f32_e32 v99, v149, v149
	v_fmac_f32_e32 v0, v96, v96
	v_fmac_f32_e32 v99, v148, v148
	v_add_f32_e32 v0, v0, v99
	v_add_f32_e32 v0, v0, v98
	ds_swizzle_b32 v98, v0 offset:swizzle(SWAP,1)
	s_waitcnt lgkmcnt(0)
	v_add_f32_e32 v0, v0, v98
	ds_swizzle_b32 v98, v0 offset:swizzle(SWAP,2)
	s_waitcnt lgkmcnt(0)
	v_add_f32_e32 v0, v0, v98
	ds_swizzle_b32 v98, v0 offset:swizzle(SWAP,4)
	s_waitcnt lgkmcnt(0)
	v_add_f32_e32 v0, v0, v98
	ds_swizzle_b32 v98, v0 offset:swizzle(SWAP,8)
	s_waitcnt lgkmcnt(0)
	v_add_f32_e32 v0, v0, v98
	ds_swizzle_b32 v98, v0 offset:swizzle(SWAP,16)
	s_waitcnt lgkmcnt(0)
	v_add_f32_e32 v0, v0, v98
	v_mov_b32_e32 v98, v0
	s_nop 1
	v_permlane32_swap_b32_e32 v0, v98
	v_add_f32_e32 v0, v0, v98
	v_fmamk_f32 v0, v0, 0x3a800000, v188
	v_cmp_gt_f32_e32 vcc, s31, v0
	v_mul_f32_e32 v98, 0x4f800000, v0
	s_nop 0
	v_cndmask_b32_e32 v0, v0, v98, vcc
	v_sqrt_f32_e32 v98, v0
	s_nop 0
	v_add_u32_e32 v99, -1, v98
	v_fma_f32 v100, -v99, v98, v0
	v_cmp_ge_f32_e64 s[4:5], 0, v100
	v_add_u32_e32 v100, 1, v98
	s_nop 0
	v_cndmask_b32_e64 v99, v98, v99, s[4:5]
	v_fma_f32 v98, -v100, v98, v0
	v_cmp_lt_f32_e64 s[4:5], 0, v98
	s_nop 1
	v_cndmask_b32_e64 v98, v99, v100, s[4:5]
	v_mul_f32_e32 v99, 0x37800000, v98
	v_cndmask_b32_e32 v98, v98, v99, vcc
	v_cmp_class_f32_e32 vcc, v0, v189
	s_nop 1
	v_cndmask_b32_e32 v0, v98, v0, vcc
	v_div_scale_f32 v98, s[0:1], v0, v0, 1.0
	v_rcp_f32_e32 v99, v98
	s_mov_b64 s[0:1], -1
	v_fma_f32 v100, -v98, v99, 1.0
	v_fmac_f32_e32 v99, v100, v99
	v_div_scale_f32 v100, vcc, 1.0, v0, 1.0
	v_mul_f32_e32 v101, v100, v99
	v_fma_f32 v102, -v98, v101, v100
	v_fmac_f32_e32 v101, v102, v99
	v_fma_f32 v98, -v98, v101, v100
	v_div_fmas_f32 v98, v98, v99, v101
	v_div_fixup_f32 v0, v98, v0, 1.0
	v_pk_mul_f32 v[92:93], v[92:93], v[0:1] op_sel_hi:[1,0]
	v_pk_mul_f32 v[90:91], v[90:91], v[0:1] op_sel_hi:[1,0]
	v_pk_fma_f32 v[98:99], v[2:3], v[92:93], v[6:7]
	v_pk_fma_f32 v[100:101], v[4:5], v[90:91], v[8:9]
	v_pk_mul_f32 v[90:91], v[140:141], v[0:1] op_sel_hi:[1,0]
	v_pk_mul_f32 v[92:93], v[94:95], v[0:1] op_sel_hi:[1,0]
	v_pk_fma_f32 v[102:103], v[10:11], v[90:91], v[14:15]
	v_pk_fma_f32 v[104:105], v[12:13], v[92:93], v[16:17]
	v_pk_mul_f32 v[90:91], v[142:143], v[0:1] op_sel_hi:[1,0]
	v_pk_mul_f32 v[92:93], v[144:145], v[0:1] op_sel_hi:[1,0]
	v_pk_mul_f32 v[94:95], v[96:97], v[0:1] op_sel_hi:[1,0]
	v_pk_mul_f32 v[96:97], v[148:149], v[0:1] op_sel_hi:[1,0]
	v_pk_fma_f32 v[92:93], v[20:21], v[92:93], v[24:25]
	v_pk_fma_f32 v[90:91], v[18:19], v[90:91], v[22:23]
	v_pk_fma_f32 v[96:97], v[28:29], v[96:97], v[32:33]
	v_pk_fma_f32 v[94:95], v[26:27], v[94:95], v[30:31]
	s_waitcnt vmcnt(0)
	s_and_b64 vcc, exec, s[2:3]
	s_cbranch_vccnz .LBB0_1212
	v_bfe_u32 v0, v98, 16, 1
	v_add3_u32 v0, v98, v0, s43
	v_bfe_u32 v107, v99, 16, 1
	v_lshrrev_b32_e32 v0, 16, v0
	v_add3_u32 v107, v99, v107, s43
	v_and_or_b32 v140, v107, s33, v0
	v_bfe_u32 v0, v100, 16, 1
	v_add3_u32 v0, v100, v0, s43
	v_bfe_u32 v107, v101, 16, 1
	v_lshrrev_b32_e32 v0, 16, v0
	v_add3_u32 v107, v101, v107, s43
	v_and_or_b32 v141, v107, s33, v0
	v_bfe_u32 v0, v102, 16, 1
	v_add3_u32 v0, v102, v0, s43
	v_bfe_u32 v107, v103, 16, 1
	v_lshrrev_b32_e32 v0, 16, v0
	v_add3_u32 v107, v103, v107, s43
	v_and_or_b32 v142, v107, s33, v0
	v_bfe_u32 v0, v104, 16, 1
	v_add3_u32 v0, v104, v0, s43
	v_bfe_u32 v107, v105, 16, 1
	v_lshrrev_b32_e32 v0, 16, v0
	v_add3_u32 v107, v105, v107, s43
	v_and_or_b32 v143, v107, s33, v0
	v_bfe_u32 v0, v90, 16, 1
	v_add_co_u32_e32 v144, vcc, s39, v138
	v_add3_u32 v0, v90, v0, s43
	v_bfe_u32 v107, v91, 16, 1
	v_addc_co_u32_e32 v145, vcc, 0, v139, vcc
	v_lshrrev_b32_e32 v0, 16, v0
	v_add3_u32 v107, v91, v107, s43
	global_store_dwordx4 v[144:145], v[140:143], off nt
	s_mov_b64 s[0:1], 0
	s_nop 0
	v_and_or_b32 v140, v107, s33, v0
	v_bfe_u32 v0, v92, 16, 1
	v_add3_u32 v0, v92, v0, s43
	v_bfe_u32 v107, v93, 16, 1
	v_lshrrev_b32_e32 v0, 16, v0
	v_add3_u32 v107, v93, v107, s43
	v_and_or_b32 v141, v107, s33, v0
	v_bfe_u32 v0, v94, 16, 1
	v_add3_u32 v0, v94, v0, s43
	v_bfe_u32 v107, v95, 16, 1
	v_lshrrev_b32_e32 v0, 16, v0
	v_add3_u32 v107, v95, v107, s43
	v_and_or_b32 v142, v107, s33, v0
	v_bfe_u32 v0, v96, 16, 1
	v_add3_u32 v0, v96, v0, s43
	v_bfe_u32 v107, v97, 16, 1
	v_lshrrev_b32_e32 v0, 16, v0
	v_add3_u32 v107, v97, v107, s43
	v_and_or_b32 v143, v107, s33, v0
	global_store_dwordx4 v[144:145], v[140:143], off offset:1024 nt
; __device__ __forceinline__ unsigned pk2(float lo, float hi) { return f2bf(lo) | (f2bf(hi) << 16); }
; __device__ __forceinline__ unsigned cvt_fp8x4(float a, float b, float c, float d) { int w = __builtin_amdgcn_cvt_pk_fp8_f32(a, b, 0, false); w = __builtin_amdgcn_cvt_pk_fp8_f32(c, d, w, true); return (unsigned)w; }
; template <int MODE, bool FIRSTX>
; __device__ __forceinline__ void row_pass(Frame& F, int layer, bool final_out, int row0) {
;     ...
;             if (final_out) { if (row >= NCTX) {
; #pragma unroll
;                 for (int q = 0; q < 4; ++q) *(f32x4*)(F.out + (size_t)(row - NCTX) * DM + RP_COL(q)) = v[q]; } }
;             else {
; #pragma unroll
;                 for (int j = 0; j < 2; ++j) { u32x4 w; w.x = pk2(v[2 * j][0], v[2 * j][1]); w.y = pk2(v[2 * j][2], v[2 * j][3]); w.z = pk2(v[2 * j + 1][0], v[2 * j + 1][1]); w.w = pk2(v[2 * j + 1][2], v[2 * j + 1][3]);
;                     *(u32x4*)(X + (size_t)row * DM + lc + 512 * j) = w; } }
;         }
;         if (!final_out) {
; #pragma unroll
;             for (int j = 0; j < 2; ++j) { const f32x4 h0 = v[2 * j] * (sc[2 * j] + 1.0f) + sh[2 * j], h1 = v[2 * j + 1] * (sc[2 * j + 1] + 1.0f) + sh[2 * j + 1];
;                 if (MODE == 1 || (nlayer % 3) == 2) { u32x4 w; w.x = pk2(h0[0], h0[1]); w.y = pk2(h0[2], h0[3]); w.z = pk2(h1[0], h1[1]); w.w = pk2(h1[2], h1[3]);
;                     *(u32x4*)(H + (size_t)row * DM + lc + 512 * j) = w; }
;                 if (MODE == 1 || (nlayer % 3) != 2) {                                u32x2 w8; w8.x = cvt_fp8x4(h0[0], h0[1], h0[2], h0[3]); w8.y = cvt_fp8x4(h1[0], h1[1], h1[2], h1[3]); *(u32x2*)(F.ws + WS_H8 + (size_t)row * DM + lc + 512 * j) = w8; } }
.LBB0_1212:
	s_andn2_b64 vcc, exec, s[0:1]
	s_cbranch_vccnz .LBB0_1215
	s_cmpk_lt_i32 s26, 0x800
	s_cbranch_scc1 .LBB0_1215
	s_lshl_b64 s[0:1], s[18:19], 12
	v_lshl_add_u64 v[140:141], v[116:117], 0, s[0:1]
	global_store_dwordx4 v[140:141], v[98:101], off nt
	global_store_dwordx4 v[140:141], v[102:105], off offset:16 nt
	global_store_dwordx4 v[140:141], v[90:93], off offset:2048 nt
	global_store_dwordx4 v[140:141], v[94:97], off offset:2064 nt
.LBB0_1215:
	s_and_b64 vcc, exec, s[2:3]
	s_cbranch_vccnz .LBB0_1200
	v_pk_add_f32 v[142:143], v[62:63], 1.0 op_sel_hi:[1,0]
	v_pk_add_f32 v[140:141], v[64:65], 1.0 op_sel_hi:[1,0]
	v_pk_fma_f32 v[142:143], v[142:143], v[98:99], v[46:47]
	v_pk_add_f32 v[98:99], v[60:61], 1.0 op_sel_hi:[1,0]
	v_pk_add_f32 v[144:145], v[58:59], 1.0 op_sel_hi:[1,0]
	v_pk_fma_f32 v[140:141], v[140:141], v[100:101], v[48:49]
	v_pk_fma_f32 v[100:101], v[98:99], v[104:105], v[44:45]
	v_pk_fma_f32 v[102:103], v[144:145], v[102:103], v[42:43]
	s_mov_b64 s[0:1], -1
	s_and_b64 vcc, exec, s[74:75]
	v_lshl_add_u64 v[98:99], s[94:95], 0, v[120:121]
	s_cbranch_vccz .LBB0_1218
	v_mov_b32_e32 v104, v1
	v_mov_b32_e32 v105, v1
	v_cvt_pk_fp8_f32 v104, v142, v143
	v_cvt_pk_fp8_f32 v105, v102, v103
	v_add_co_u32_e32 v144, vcc, 0x99000000, v98
	v_cvt_pk_fp8_f32 v104, v140, v141 op_sel:[0,0,1]
	v_cvt_pk_fp8_f32 v105, v100, v101 op_sel:[0,0,1]
	v_addc_co_u32_e32 v145, vcc, 0, v99, vcc
	s_mov_b64 s[0:1], 0
	global_store_dwordx2 v[144:145], v[104:105], off nt
.LBB0_1218:
	s_andn2_b64 vcc, exec, s[0:1]
	s_cbranch_vccnz .LBB0_1220
	v_bfe_u32 v0, v142, 16, 1
	v_add3_u32 v0, v142, v0, s43
	v_bfe_u32 v104, v143, 16, 1
	v_lshrrev_b32_e32 v0, 16, v0
	v_add3_u32 v104, v143, v104, s43
	v_and_or_b32 v142, v104, s33, v0
	v_bfe_u32 v0, v140, 16, 1
	v_add3_u32 v0, v140, v0, s43
	v_bfe_u32 v104, v141, 16, 1
	v_lshrrev_b32_e32 v0, 16, v0
	v_add3_u32 v104, v141, v104, s43
	v_and_or_b32 v143, v104, s33, v0
	v_bfe_u32 v0, v102, 16, 1
	v_add3_u32 v0, v102, v0, s43
	v_bfe_u32 v102, v103, 16, 1
	v_lshrrev_b32_e32 v0, 16, v0
	v_add3_u32 v102, v103, v102, s43
	v_and_or_b32 v144, v102, s33, v0
	v_bfe_u32 v0, v100, 16, 1
	v_add3_u32 v0, v100, v0, s43
	v_bfe_u32 v100, v101, 16, 1
	v_lshrrev_b32_e32 v0, 16, v0
	v_add3_u32 v100, v101, v100, s43
	v_and_or_b32 v145, v100, s33, v0
	v_add_co_u32_e32 v100, vcc, 0x44c00000, v138
	s_nop 1
	v_addc_co_u32_e32 v101, vcc, 0, v139, vcc
	global_store_dwordx4 v[100:101], v[142:145], off nt
.LBB0_1220:
	v_pk_add_f32 v[100:101], v[56:57], 1.0 op_sel_hi:[1,0]
	v_pk_add_f32 v[102:103], v[54:55], 1.0 op_sel_hi:[1,0]
	v_pk_fma_f32 v[92:93], v[100:101], v[92:93], v[40:41]
	v_pk_fma_f32 v[100:101], v[102:103], v[90:91], v[38:39]
	v_pk_add_f32 v[90:91], v[52:53], 1.0 op_sel_hi:[1,0]
	v_pk_add_f32 v[102:103], v[50:51], 1.0 op_sel_hi:[1,0]
	v_pk_fma_f32 v[90:91], v[90:91], v[96:97], v[36:37]
	v_pk_fma_f32 v[94:95], v[102:103], v[94:95], v[34:35]
	s_andn2_b64 vcc, exec, s[74:75]
	s_mov_b64 s[0:1], -1
	s_cbranch_vccnz .LBB0_1222
	v_mov_b32_e32 v96, v1
	v_mov_b32_e32 v97, v1
	v_cvt_pk_fp8_f32 v96, v100, v101
	v_cvt_pk_fp8_f32 v97, v94, v95
	v_add_co_u32_e32 v98, vcc, 0x99000000, v98
	v_cvt_pk_fp8_f32 v96, v92, v93 op_sel:[0,0,1]
	v_cvt_pk_fp8_f32 v97, v90, v91 op_sel:[0,0,1]
	v_addc_co_u32_e32 v99, vcc, 0, v99, vcc
	s_mov_b64 s[0:1], 0
	global_store_dwordx2 v[98:99], v[96:97], off offset:512 nt
.LBB0_1222:
	s_andn2_b64 vcc, exec, s[0:1]
	s_cbranch_vccnz .LBB0_1200
	v_bfe_u32 v0, v100, 16, 1
	v_add3_u32 v0, v100, v0, s43
	v_bfe_u32 v96, v101, 16, 1
	v_lshrrev_b32_e32 v0, 16, v0
	v_add3_u32 v96, v101, v96, s43
	v_and_or_b32 v96, v96, s33, v0
	v_bfe_u32 v0, v92, 16, 1
	v_add3_u32 v0, v92, v0, s43
	v_bfe_u32 v92, v93, 16, 1
	v_lshrrev_b32_e32 v0, 16, v0
	v_add3_u32 v92, v93, v92, s43
	v_and_or_b32 v97, v92, s33, v0
	v_bfe_u32 v0, v94, 16, 1
	v_add3_u32 v0, v94, v0, s43
	v_bfe_u32 v92, v95, 16, 1
	v_lshrrev_b32_e32 v0, 16, v0
	v_add3_u32 v92, v95, v92, s43
	v_and_or_b32 v98, v92, s33, v0
	v_bfe_u32 v0, v90, 16, 1
	v_add3_u32 v0, v90, v0, s43
	v_bfe_u32 v90, v91, 16, 1
	v_lshrrev_b32_e32 v0, 16, v0
	v_add3_u32 v90, v91, v90, s43
	v_and_or_b32 v99, v90, s33, v0
	v_add_co_u32_e32 v90, vcc, 0x44c00000, v138
	s_nop 1
	v_addc_co_u32_e32 v91, vcc, 0, v139, vcc
	global_store_dwordx4 v[90:91], v[96:99], off offset:1024 nt
	s_branch .LBB0_1200
